# grid barrier rewritten: non-returning arrival adds, fixed per-XCD leader polls its counter, all workgroups poll the top counter (no returning atomics, no relay)
# speedup vs baseline: 1.0027x; 1.0027x over previous
.LBB0_146:
	v_readlane_b32 s0, v251, 3
	s_add_i32 s16, s97, 2
	v_readlane_b32 s3, v251, 6
	s_cmp_ge_i32 s16, s3
	s_waitcnt vmcnt(0)
	s_barrier
	v_readlane_b32 s1, v251, 4
	v_readlane_b32 s2, v251, 5
	s_cbranch_scc1 .LBB0_196
	s_waitcnt vmcnt(0)
	s_barrier
	s_mov_b64 s[0:1], exec
	v_readlane_b32 s2, v251, 7
	v_readlane_b32 s3, v251, 8
	s_and_b64 s[2:3], s[0:1], s[2:3]
	s_mov_b64 exec, s[2:3]
	s_cbranch_execz .LBB0_195
	v_readlane_b32 s2, v252, 33
	v_readlane_b32 s4, v252, 15
	v_readlane_b32 s5, v252, 16
	v_readlane_b32 s6, v252, 19
	v_readlane_b32 s7, v252, 20
	s_waitcnt vmcnt(0) expcnt(0) lgkmcnt(0)
	v_mov_b32_e32 v0, s2
	ds_read_b128 v[2:5], v0
	s_waitcnt lgkmcnt(0)
	v_readfirstlane_b32 s8, v2
	v_readfirstlane_b32 s9, v3
	v_readfirstlane_b32 s10, v4
	v_readfirstlane_b32 s11, v5
	s_add_i32 s11, s11, 1
	s_add_i32 s12, s11, 1
	s_mul_i32 s13, s12, s8
	s_mul_i32 s14, s12, s9
	s_cmp_lg_u32 s10, 0
	s_cbranch_scc1 .Lnb_hl_0
	global_atomic_add v2, v1, v204, s[4:5] offset:4 sc0
	s_waitcnt vmcnt(0)
	v_readfirstlane_b32 s10, v2
	s_cmp_eq_u32 s10, 0
	s_cselect_b32 s10, 1, 2
.Lnb_hl_0:
	global_atomic_add v1, v204, s[4:5]
	s_cmp_lg_u32 s10, 1
	s_cbranch_scc1 .Lnb_mem_0
	s_mov_b32 s15, 0
.Lnb_lp_0:
	global_load_dword v2, v1, s[4:5] sc1
	s_waitcnt vmcnt(0)
	v_readfirstlane_b32 s12, v2
	s_cmp_ge_u32 s12, s13
	s_cbranch_scc1 .Lnb_ld_0
	s_add_i32 s15, s15, 1
	s_cmp_lt_u32 s15, 0x8000
	s_cbranch_scc1 .Lnb_lp_0
.Lnb_ld_0:
	buffer_wbl2 sc1
	s_waitcnt vmcnt(0)
	global_atomic_add v1, v204, s[6:7]
.Lnb_mem_0:
	s_mov_b32 s15, 0
.Lnb_tp_0:
	global_load_dword v2, v1, s[6:7] sc1
	s_waitcnt vmcnt(0)
	v_readfirstlane_b32 s12, v2
	s_cmp_ge_u32 s12, s14
	s_cbranch_scc1 .Lnb_td_0
	s_sleep 1
	s_add_i32 s15, s15, 1
	s_cmp_lt_u32 s15, 0x8000
	s_cbranch_scc1 .Lnb_tp_0
.Lnb_td_0:
	buffer_inv sc1
	v_mov_b32_e32 v2, s10
	v_mov_b32_e32 v3, s11
	ds_write2_b32 v0, v2, v3 offset0:2 offset1:3
	s_waitcnt vmcnt(0) lgkmcnt(0)

.LBB0_542:
	v_readlane_b32 s0, v251, 3
	s_add_i32 s16, s97, 3
	v_readlane_b32 s3, v251, 6
	s_cmp_ge_i32 s16, s3
	s_barrier
	v_readlane_b32 s1, v251, 4
	v_readlane_b32 s2, v251, 5
	s_cbranch_scc1 .LBB0_554
	s_waitcnt vmcnt(0)
	s_barrier
	s_mov_b64 s[0:1], exec
	v_readlane_b32 s2, v251, 7
	v_readlane_b32 s3, v251, 8
	s_and_b64 s[2:3], s[0:1], s[2:3]
	s_movk_i32 s33, 0x4000
	s_movk_i32 s40, 0x90
	s_movk_i32 s48, 0x5ff
	s_movk_i32 s94, 0xfff
	s_movk_i32 s38, 0x1000
	v_readlane_b32 s96, v253, 58
	v_readlane_b32 s41, v253, 59
	s_movk_i32 s43, 0xa000
	s_mov_b64 exec, s[2:3]
	s_cbranch_execz .LBB0_592
	v_readlane_b32 s2, v252, 33
	v_readlane_b32 s4, v252, 15
	v_readlane_b32 s5, v252, 16
	v_readlane_b32 s6, v252, 19
	v_readlane_b32 s7, v252, 20
	s_waitcnt vmcnt(0) expcnt(0) lgkmcnt(0)
	v_mov_b32_e32 v0, s2
	ds_read_b128 v[2:5], v0
	s_waitcnt lgkmcnt(0)
	v_readfirstlane_b32 s8, v2
	v_readfirstlane_b32 s9, v3
	v_readfirstlane_b32 s10, v4
	v_readfirstlane_b32 s11, v5
	s_add_i32 s11, s11, 1
	s_add_i32 s12, s11, 1
	s_mul_i32 s13, s12, s8
	s_mul_i32 s14, s12, s9
	s_cmp_lg_u32 s10, 0
	s_cbranch_scc1 .Lnb_hl_1
	global_atomic_add v2, v1, v204, s[4:5] offset:4 sc0
	s_waitcnt vmcnt(0)
	v_readfirstlane_b32 s10, v2
	s_cmp_eq_u32 s10, 0
	s_cselect_b32 s10, 1, 2

.Lnb_td_1:
	buffer_inv sc1
	v_mov_b32_e32 v2, s10
	v_mov_b32_e32 v3, s11
	ds_write2_b32 v0, v2, v3 offset0:2 offset1:3
	s_waitcnt vmcnt(0) lgkmcnt(0)
	s_branch .LBB0_592
.LBB0_554:
	s_movk_i32 s33, 0x4000
	s_movk_i32 s40, 0x90
	s_movk_i32 s48, 0x5ff
	s_movk_i32 s94, 0xfff
	s_movk_i32 s38, 0x1000
	v_readlane_b32 s96, v253, 58
	v_readlane_b32 s41, v253, 59
	s_movk_i32 s43, 0xa000
	s_branch .LBB0_593
.LBB0_592:
	s_or_b64 exec, exec, s[0:1]
	s_waitcnt lgkmcnt(0)
	s_barrier

.LBB0_669:
	s_or_b64 exec, exec, s[12:13]
	v_readlane_b32 s0, v251, 3
	s_add_i32 s16, s97, 4
	v_readlane_b32 s3, v251, 6
	s_cmp_ge_i32 s16, s3
	s_movk_i32 s33, 0x4000
	s_movk_i32 s38, 0x1000
	s_waitcnt lgkmcnt(0)
	s_barrier
	v_readlane_b32 s1, v251, 4
	v_readlane_b32 s2, v251, 5
	s_cbranch_scc1 .LBB0_719
	s_waitcnt vmcnt(0)
	s_barrier
	s_mov_b64 s[0:1], exec
	v_readlane_b32 s2, v251, 7
	v_readlane_b32 s3, v251, 8
	s_and_b64 s[2:3], s[0:1], s[2:3]
	s_mov_b64 exec, s[2:3]
	s_cbranch_execz .LBB0_718
	v_readlane_b32 s2, v252, 33
	v_readlane_b32 s4, v252, 15
	v_readlane_b32 s5, v252, 16
	v_readlane_b32 s6, v252, 19
	v_readlane_b32 s7, v252, 20
	s_waitcnt vmcnt(0) expcnt(0) lgkmcnt(0)
	v_mov_b32_e32 v0, s2
	ds_read_b128 v[2:5], v0
	s_waitcnt lgkmcnt(0)
	v_readfirstlane_b32 s8, v2
	v_readfirstlane_b32 s9, v3
	v_readfirstlane_b32 s10, v4
	v_readfirstlane_b32 s11, v5
	s_add_i32 s11, s11, 1
	s_add_i32 s12, s11, 1
	s_mul_i32 s13, s12, s8
	s_mul_i32 s14, s12, s9
	s_cmp_lg_u32 s10, 0
	s_cbranch_scc1 .Lnb_hl_2
	global_atomic_add v2, v1, v204, s[4:5] offset:4 sc0
	s_waitcnt vmcnt(0)
	v_readfirstlane_b32 s10, v2
	s_cmp_eq_u32 s10, 0
	s_cselect_b32 s10, 1, 2

.LBB0_1148:
	v_readlane_b32 s0, v251, 3
	s_add_i32 s16, s97, 5
	v_readlane_b32 s3, v251, 6
	s_cmp_ge_i32 s16, s3
	v_readlane_b32 s1, v251, 4
	v_readlane_b32 s2, v251, 5
	s_cbranch_scc1 .LBB0_1198
	s_waitcnt vmcnt(0)
	s_barrier
	s_mov_b64 s[0:1], exec
	v_readlane_b32 s2, v251, 7
	v_readlane_b32 s3, v251, 8
	s_and_b64 s[2:3], s[0:1], s[2:3]
	s_mov_b64 exec, s[2:3]
	s_cbranch_execz .LBB0_1197
	v_readlane_b32 s2, v252, 33
	v_readlane_b32 s4, v252, 15
	v_readlane_b32 s5, v252, 16
	v_readlane_b32 s6, v252, 19
	v_readlane_b32 s7, v252, 20
	s_waitcnt vmcnt(0) expcnt(0) lgkmcnt(0)
	v_mov_b32_e32 v0, s2
	ds_read_b128 v[2:5], v0
	s_waitcnt lgkmcnt(0)
	v_readfirstlane_b32 s8, v2
	v_readfirstlane_b32 s9, v3
	v_readfirstlane_b32 s10, v4
	v_readfirstlane_b32 s11, v5
	s_add_i32 s11, s11, 1
	s_add_i32 s12, s11, 1
	s_mul_i32 s13, s12, s8
	s_mul_i32 s14, s12, s9
	s_cmp_lg_u32 s10, 0
	s_cbranch_scc1 .Lnb_hl_3
	global_atomic_add v2, v1, v204, s[4:5] offset:4 sc0
	s_waitcnt vmcnt(0)
	v_readfirstlane_b32 s10, v2
	s_cmp_eq_u32 s10, 0
	s_cselect_b32 s10, 1, 2

.LBB0_1251:
	v_readlane_b32 s0, v251, 3
	s_add_i32 s16, s97, 6
	v_readlane_b32 s3, v251, 6
	s_cmp_ge_i32 s16, s3
	v_readlane_b32 s1, v251, 4
	v_readlane_b32 s2, v251, 5
	s_cbranch_scc1 .LBB0_1301
	s_waitcnt vmcnt(0)
	s_barrier
	s_mov_b64 s[0:1], exec
	v_readlane_b32 s2, v251, 7
	v_readlane_b32 s3, v251, 8
	s_and_b64 s[2:3], s[0:1], s[2:3]
	s_mov_b64 exec, s[2:3]
	s_cbranch_execz .LBB0_1300
	v_readlane_b32 s2, v252, 33
	v_readlane_b32 s4, v252, 15
	v_readlane_b32 s5, v252, 16
	v_readlane_b32 s6, v252, 19
	v_readlane_b32 s7, v252, 20
	s_waitcnt vmcnt(0) expcnt(0) lgkmcnt(0)
	v_mov_b32_e32 v0, s2
	ds_read_b128 v[2:5], v0
	s_waitcnt lgkmcnt(0)
	v_readfirstlane_b32 s8, v2
	v_readfirstlane_b32 s9, v3
	v_readfirstlane_b32 s10, v4
	v_readfirstlane_b32 s11, v5
	s_add_i32 s11, s11, 1
	s_add_i32 s12, s11, 1
	s_mul_i32 s13, s12, s8
	s_mul_i32 s14, s12, s9
	s_cmp_lg_u32 s10, 0
	s_cbranch_scc1 .Lnb_hl_4
	global_atomic_add v2, v1, v204, s[4:5] offset:4 sc0
	s_waitcnt vmcnt(0)
	v_readfirstlane_b32 s10, v2
	s_cmp_eq_u32 s10, 0
	s_cselect_b32 s10, 1, 2

.LBB0_1330:
	v_readlane_b32 s0, v251, 3
	s_add_i32 s16, s97, 7
	v_readlane_b32 s3, v251, 6
	s_cmp_ge_i32 s16, s3
	s_waitcnt vmcnt(0) lgkmcnt(0)
	s_barrier
	v_readlane_b32 s1, v251, 4
	v_readlane_b32 s2, v251, 5
	s_cbranch_scc1 .LBB0_1380
	s_waitcnt vmcnt(0)
	s_barrier
	s_mov_b64 s[0:1], exec
	v_readlane_b32 s2, v251, 7
	v_readlane_b32 s3, v251, 8
	s_and_b64 s[2:3], s[0:1], s[2:3]
	s_mov_b64 exec, s[2:3]
	s_cbranch_execz .LBB0_1379
	v_readlane_b32 s2, v252, 33
	v_readlane_b32 s4, v252, 15
	v_readlane_b32 s5, v252, 16
	v_readlane_b32 s6, v252, 19
	v_readlane_b32 s7, v252, 20
	s_waitcnt vmcnt(0) expcnt(0) lgkmcnt(0)
	v_mov_b32_e32 v0, s2
	ds_read_b128 v[2:5], v0
	s_waitcnt lgkmcnt(0)
	v_readfirstlane_b32 s8, v2
	v_readfirstlane_b32 s9, v3
	v_readfirstlane_b32 s10, v4
	v_readfirstlane_b32 s11, v5
	s_add_i32 s11, s11, 1
	s_add_i32 s12, s11, 1
	s_mul_i32 s13, s12, s8
	s_mul_i32 s14, s12, s9
	s_cmp_lg_u32 s10, 0
	s_cbranch_scc1 .Lnb_hl_5
	global_atomic_add v2, v1, v204, s[4:5] offset:4 sc0
	s_waitcnt vmcnt(0)
	v_readfirstlane_b32 s10, v2
	s_cmp_eq_u32 s10, 0
	s_cselect_b32 s10, 1, 2

.LBB0_1778:
	v_readlane_b32 s0, v251, 3
	s_add_i32 s16, s97, 8
	v_readlane_b32 s3, v251, 6
	s_cmp_ge_i32 s16, s3
	s_barrier
	v_readlane_b32 s1, v251, 4
	v_readlane_b32 s2, v251, 5
	s_cbranch_scc1 .LBB0_1828
	s_waitcnt vmcnt(0)
	s_barrier
	s_mov_b64 s[0:1], exec
	v_readlane_b32 s2, v251, 7
	v_readlane_b32 s3, v251, 8
	s_and_b64 s[2:3], s[0:1], s[2:3]
	s_mov_b64 exec, s[2:3]
	s_cbranch_execz .LBB0_1827
	v_readlane_b32 s2, v252, 33
	v_readlane_b32 s4, v252, 15
	v_readlane_b32 s5, v252, 16
	v_readlane_b32 s6, v252, 19
	v_readlane_b32 s7, v252, 20
	s_waitcnt vmcnt(0) expcnt(0) lgkmcnt(0)
	v_mov_b32_e32 v0, s2
	ds_read_b128 v[2:5], v0
	s_waitcnt lgkmcnt(0)
	v_readfirstlane_b32 s8, v2
	v_readfirstlane_b32 s9, v3
	v_readfirstlane_b32 s10, v4
	v_readfirstlane_b32 s11, v5
	s_add_i32 s11, s11, 1
	s_add_i32 s12, s11, 1
	s_mul_i32 s13, s12, s8
	s_mul_i32 s14, s12, s9
	s_cmp_lg_u32 s10, 0
	s_cbranch_scc1 .Lnb_hl_6
	global_atomic_add v2, v1, v204, s[4:5] offset:4 sc0
	s_waitcnt vmcnt(0)
	v_readfirstlane_b32 s10, v2
	s_cmp_eq_u32 s10, 0
	s_cselect_b32 s10, 1, 2

.LBB0_1877:
	v_readlane_b32 s0, v251, 3
	s_add_i32 s16, s97, 9
	v_readlane_b32 s3, v251, 6
	s_cmp_ge_i32 s16, s3
	s_barrier
	v_readlane_b32 s1, v251, 4
	v_readlane_b32 s2, v251, 5
	s_cbranch_scc1 .LBB0_1927
	s_waitcnt vmcnt(0)
	s_barrier
	s_mov_b64 s[0:1], exec
	v_readlane_b32 s2, v251, 7
	v_readlane_b32 s3, v251, 8
	s_and_b64 s[2:3], s[0:1], s[2:3]
	s_mov_b64 exec, s[2:3]
	s_cbranch_execz .LBB0_1926
	v_readlane_b32 s2, v252, 33
	v_readlane_b32 s4, v252, 15
	v_readlane_b32 s5, v252, 16
	v_readlane_b32 s6, v252, 19
	v_readlane_b32 s7, v252, 20
	s_waitcnt vmcnt(0) expcnt(0) lgkmcnt(0)
	v_mov_b32_e32 v0, s2
	ds_read_b128 v[2:5], v0
	s_waitcnt lgkmcnt(0)
	v_readfirstlane_b32 s8, v2
	v_readfirstlane_b32 s9, v3
	v_readfirstlane_b32 s10, v4
	v_readfirstlane_b32 s11, v5
	s_add_i32 s11, s11, 1
	s_add_i32 s12, s11, 1
	s_mul_i32 s13, s12, s8
	s_mul_i32 s14, s12, s9
	s_cmp_lg_u32 s10, 0
	s_cbranch_scc1 .Lnb_hl_7
	global_atomic_add v2, v1, v204, s[4:5] offset:4 sc0
	s_waitcnt vmcnt(0)
	v_readfirstlane_b32 s10, v2
	s_cmp_eq_u32 s10, 0
	s_cselect_b32 s10, 1, 2

.LBB0_2085:
	v_readlane_b32 s0, v251, 3
	s_add_i32 s16, s97, 10
	v_readlane_b32 s3, v251, 6
	s_cmp_ge_i32 s16, s3
	s_waitcnt vmcnt(0) lgkmcnt(0)
	s_barrier
	v_readlane_b32 s1, v251, 4
	v_readlane_b32 s2, v251, 5
	s_cbranch_scc1 .LBB0_2137
	s_waitcnt vmcnt(0)
	s_barrier
	s_mov_b64 s[0:1], exec
	v_readlane_b32 s2, v251, 7
	v_readlane_b32 s3, v251, 8
	s_and_b64 s[2:3], s[0:1], s[2:3]
	s_mov_b64 exec, s[2:3]
	s_cbranch_execz .LBB0_2136
	v_readlane_b32 s2, v252, 33
	v_readlane_b32 s4, v252, 15
	v_readlane_b32 s5, v252, 16
	v_readlane_b32 s6, v252, 19
	v_readlane_b32 s7, v252, 20
	s_waitcnt vmcnt(0) expcnt(0) lgkmcnt(0)
	v_mov_b32_e32 v0, s2
	ds_read_b128 v[2:5], v0
	s_waitcnt lgkmcnt(0)
	v_readfirstlane_b32 s8, v2
	v_readfirstlane_b32 s9, v3
	v_readfirstlane_b32 s10, v4
	v_readfirstlane_b32 s11, v5
	s_add_i32 s11, s11, 1
	s_add_i32 s12, s11, 1
	s_mul_i32 s13, s12, s8
	s_mul_i32 s14, s12, s9
	s_cmp_lg_u32 s10, 0
	s_cbranch_scc1 .Lnb_hl_8
	global_atomic_add v2, v1, v204, s[4:5] offset:4 sc0
	s_waitcnt vmcnt(0)
	v_readfirstlane_b32 s10, v2
	s_cmp_eq_u32 s10, 0
	s_cselect_b32 s10, 1, 2

.LBB0_2098:
	v_ashrrev_i32_e32 v9, 31, v8
	v_lshl_add_u64 v[4:5], v[8:9], 2, s[16:17]
	global_load_dword v8, v[4:5], off
	s_and_b64 vcc, exec, s[0:1]
	v_add_u32_e32 v4, s11, v175
	s_movk_i32 s83, 0x1000
	s_cbranch_vccz .LBB0_2027
	s_branch .LBB0_2028
.LBB0_2136:
	s_or_b64 exec, exec, s[0:1]
	s_waitcnt lgkmcnt(0)
	s_barrier

.LBB0_2165:
	v_readlane_b32 s2, v252, 33
	v_readlane_b32 s4, v252, 15
	v_readlane_b32 s5, v252, 16
	v_readlane_b32 s6, v252, 19
	v_readlane_b32 s7, v252, 20
	s_waitcnt vmcnt(0) expcnt(0) lgkmcnt(0)
	v_mov_b32_e32 v0, s2
	ds_read_b128 v[2:5], v0
	s_waitcnt lgkmcnt(0)
	v_readfirstlane_b32 s8, v2
	v_readfirstlane_b32 s9, v3
	v_readfirstlane_b32 s10, v4
	v_readfirstlane_b32 s11, v5
	s_add_i32 s11, s11, 1
	s_add_i32 s12, s11, 1
	s_mul_i32 s13, s12, s8
	s_mul_i32 s14, s12, s9
	s_cmp_lg_u32 s10, 0
	s_cbranch_scc1 .Lnb_hl_9
	global_atomic_add v2, v1, v204, s[4:5] offset:4 sc0
	s_waitcnt vmcnt(0)
	v_readfirstlane_b32 s10, v2
	s_cmp_eq_u32 s10, 0
	s_cselect_b32 s10, 1, 2

.Lnb_td_9:
	buffer_inv sc1
	v_mov_b32_e32 v2, s10
	v_mov_b32_e32 v3, s11
	ds_write2_b32 v0, v2, v3 offset0:2 offset1:3
	s_waitcnt vmcnt(0) lgkmcnt(0)
	s_getpc_b64 s[98:99]
